# MoE down-projection epilogue: the per-slot expert outputs are written once and read once, so their 32 store sites carry the nt (streaming) hint; plus previous changes
# baseline (speedup 1.0000x reference)
; __device__ __forceinline__ unsigned cvt_pk_bf16(float lo, float hi) { unsigned r; asm volatile("v_cvt_pk_bf16_f32 %0, %1, %2" : "=v"(r) : "v"(lo), "v"(hi)); return r; }
;     __device__ __forceinline__ int* rtok() const { return (int*)(ws + WS_RTOK); }
;     __device__ __forceinline__ float* rw() const { return (float*)(ws + WS_RW); }
;     __device__ __forceinline__ bf16_t* Y() const { return (bf16_t*)(ws + WS_Y); }
;     __device__ __forceinline__ void operator()(const AccT& acc, const gm::GUnit& u, int wr, int wc, int fr, int fq) const {
;     ...
;             const int col = u.pn * 256 + wc * 32 + 8 * fq;
;             f32x4 bv[2][2];
; #pragma unroll
;             for (int bj = 0; bj < 2; ++bj) { bv[bj][0] = *(const f32x4*)(bd + u.e * 1024 + col + bj * 128); bv[bj][1] = *(const f32x4*)(bd + u.e * 1024 + col + bj * 128 + 4); }
;             int slots[8]; float ws8[8];
; #pragma unroll
;             for (int i = 0; i < 8; ++i) { const int row = u.pm * 256 + (i >> 2) * 128 + wr * 64 + (i & 3) * 16 + fr; slots[i] = rtok[row]; ws8[i] = rw[row]; }
;             __builtin_amdgcn_sched_barrier(0);
; #pragma unroll
;             for (int ai = 0; ai < 2; ++ai)
; #pragma unroll
;                 for (int m = 0; m < 4; ++m) {
;                     const int slot = slots[ai * 4 + m];
;                     if (slot >= 0) {
;                         const float w = ws8[ai * 4 + m];
;                         bf16_t* yp = Y + (size_t)slot * DM + col;
; #pragma unroll
;                         for (int bj = 0; bj < 2; ++bj) {
;                             const f32x4 y0 = (acc[ai][bj][m][0] + bv[bj][0]) * w, y1 = (acc[ai][bj][m][1] + bv[bj][1]) * w;
;                             u32x4 q; q.x = cvt_pk_bf16(y0[0], y0[1]); q.y = cvt_pk_bf16(y0[2], y0[3]); q.z = cvt_pk_bf16(y1[0], y1[1]); q.w = cvt_pk_bf16(y1[2], y1[3]);
;                             *(u32x4*)(yp + bj * 128) = q;
;                         }
;                     }
;                 }
.LBB0_1814:
	v_mov_b32_e32 v191, v147
	v_lshlrev_b64 v[190:191], 11, v[190:191]
	v_lshl_add_u64 v[190:191], s[44:45], 0, v[190:191]
	v_lshl_add_u64 v[194:195], v[148:149], 1, v[190:191]
	v_pk_add_f32 v[190:191], v[136:137], v[144:145]
	v_pk_add_f32 v[192:193], v[134:135], v[142:143]
	v_pk_mul_f32 v[200:201], v[190:191], v[178:179] op_sel_hi:[1,0]
	v_pk_mul_f32 v[190:191], v[192:193], v[178:179] op_sel_hi:[1,0]
	v_pk_add_f32 v[192:193], v[132:133], v[140:141]
	v_pk_add_f32 v[202:203], v[130:131], v[138:139]
	v_pk_mul_f32 v[204:205], v[192:193], v[178:179] op_sel_hi:[1,0]
	v_pk_mul_f32 v[192:193], v[202:203], v[178:179] op_sel_hi:[1,0]
	v_cvt_pk_bf16_f32 v190, v190, v191
	v_cvt_pk_bf16_f32 v191, v200, v201
	v_pk_add_f32 v[202:203], v[58:59], v[122:123]
	v_cvt_pk_bf16_f32 v192, v192, v193
	v_cvt_pk_bf16_f32 v193, v204, v205
	global_store_dwordx4 v[194:195], v[190:193], off nt
	s_nop 1
	v_pk_add_f32 v[190:191], v[64:65], v[128:129]
	v_pk_add_f32 v[192:193], v[62:63], v[126:127]
	v_pk_mul_f32 v[200:201], v[190:191], v[178:179] op_sel_hi:[1,0]
	v_pk_mul_f32 v[190:191], v[192:193], v[178:179] op_sel_hi:[1,0]
	v_pk_add_f32 v[192:193], v[60:61], v[124:125]
	v_cvt_pk_bf16_f32 v190, v190, v191
	v_cvt_pk_bf16_f32 v191, v200, v201
	s_nop 0
	v_pk_mul_f32 v[204:205], v[192:193], v[178:179] op_sel_hi:[1,0]
	v_pk_mul_f32 v[178:179], v[202:203], v[178:179] op_sel_hi:[1,0]
	s_nop 0
	v_cvt_pk_bf16_f32 v192, v178, v179
	v_cvt_pk_bf16_f32 v193, v204, v205
	global_store_dwordx4 v[194:195], v[190:193], off offset:256 nt
	s_or_b64 exec, exec, s[8:9]
	v_cmp_lt_i32_e32 vcc, -1, v176
	s_and_saveexec_b64 s[8:9], vcc
	s_cbranch_execz .LBB0_1803
.LBB0_1815:
	v_mov_b32_e32 v177, v147
	v_lshlrev_b64 v[176:177], 11, v[176:177]
	v_lshl_add_u64 v[176:177], s[44:45], 0, v[176:177]
	v_lshl_add_u64 v[190:191], v[148:149], 1, v[176:177]
	v_pk_add_f32 v[176:177], v[120:121], v[144:145]
	v_pk_add_f32 v[178:179], v[118:119], v[142:143]
	v_pk_mul_f32 v[192:193], v[176:177], v[174:175] op_sel_hi:[1,0]
	v_pk_mul_f32 v[176:177], v[178:179], v[174:175] op_sel_hi:[1,0]
	v_pk_add_f32 v[178:179], v[116:117], v[140:141]
	v_pk_add_f32 v[194:195], v[114:115], v[138:139]
	v_pk_mul_f32 v[200:201], v[178:179], v[174:175] op_sel_hi:[1,0]
	v_pk_mul_f32 v[178:179], v[194:195], v[174:175] op_sel_hi:[1,0]
	v_cvt_pk_bf16_f32 v176, v176, v177
	v_cvt_pk_bf16_f32 v177, v192, v193
	v_pk_add_f32 v[192:193], v[52:53], v[124:125]
	v_cvt_pk_bf16_f32 v178, v178, v179
	v_cvt_pk_bf16_f32 v179, v200, v201
	global_store_dwordx4 v[190:191], v[176:179], off nt
	v_pk_add_f32 v[194:195], v[50:51], v[122:123]
	v_pk_mul_f32 v[192:193], v[192:193], v[174:175] op_sel_hi:[1,0]
	v_pk_add_f32 v[176:177], v[56:57], v[128:129]
	v_pk_add_f32 v[178:179], v[54:55], v[126:127]
	v_pk_mul_f32 v[176:177], v[176:177], v[174:175] op_sel_hi:[1,0]
	v_pk_mul_f32 v[178:179], v[178:179], v[174:175] op_sel_hi:[1,0]
	v_pk_mul_f32 v[194:195], v[194:195], v[174:175] op_sel_hi:[1,0]
	v_cvt_pk_bf16_f32 v174, v178, v179
	v_cvt_pk_bf16_f32 v175, v176, v177
	s_nop 0
	v_cvt_pk_bf16_f32 v176, v194, v195
	v_cvt_pk_bf16_f32 v177, v192, v193
	global_store_dwordx4 v[190:191], v[174:177], off offset:256 nt
	s_or_b64 exec, exec, s[8:9]
	v_cmp_lt_i32_e32 vcc, -1, v172
	s_and_saveexec_b64 s[8:9], vcc
	s_cbranch_execz .LBB0_1804
.LBB0_1816:
	v_mov_b32_e32 v173, v147
	v_lshlrev_b64 v[172:173], 11, v[172:173]
	v_lshl_add_u64 v[172:173], s[44:45], 0, v[172:173]
	v_lshl_add_u64 v[176:177], v[148:149], 1, v[172:173]
	v_pk_add_f32 v[172:173], v[112:113], v[144:145]
	v_pk_add_f32 v[174:175], v[110:111], v[142:143]
	v_pk_mul_f32 v[178:179], v[172:173], v[170:171] op_sel_hi:[1,0]
	v_pk_mul_f32 v[172:173], v[174:175], v[170:171] op_sel_hi:[1,0]
	v_pk_add_f32 v[174:175], v[108:109], v[140:141]
	v_pk_add_f32 v[190:191], v[106:107], v[138:139]
	v_pk_mul_f32 v[192:193], v[174:175], v[170:171] op_sel_hi:[1,0]
	v_pk_mul_f32 v[174:175], v[190:191], v[170:171] op_sel_hi:[1,0]
	v_cvt_pk_bf16_f32 v172, v172, v173
	v_cvt_pk_bf16_f32 v173, v178, v179
	v_pk_add_f32 v[178:179], v[44:45], v[124:125]
	v_cvt_pk_bf16_f32 v174, v174, v175
	v_cvt_pk_bf16_f32 v175, v192, v193
	global_store_dwordx4 v[176:177], v[172:175], off nt
	v_pk_add_f32 v[190:191], v[42:43], v[122:123]
	v_pk_mul_f32 v[178:179], v[178:179], v[170:171] op_sel_hi:[1,0]
	v_pk_add_f32 v[172:173], v[48:49], v[128:129]
	v_pk_add_f32 v[174:175], v[46:47], v[126:127]
	v_pk_mul_f32 v[172:173], v[172:173], v[170:171] op_sel_hi:[1,0]
	v_pk_mul_f32 v[174:175], v[174:175], v[170:171] op_sel_hi:[1,0]
	v_pk_mul_f32 v[190:191], v[190:191], v[170:171] op_sel_hi:[1,0]
	v_cvt_pk_bf16_f32 v170, v174, v175
	v_cvt_pk_bf16_f32 v171, v172, v173
	s_nop 0
	v_cvt_pk_bf16_f32 v172, v190, v191
	v_cvt_pk_bf16_f32 v173, v178, v179
	global_store_dwordx4 v[176:177], v[170:173], off offset:256 nt
	s_or_b64 exec, exec, s[8:9]
	v_cmp_lt_i32_e32 vcc, -1, v168
	s_and_saveexec_b64 s[8:9], vcc
	s_cbranch_execz .LBB0_1805
; __device__ __forceinline__ unsigned cvt_pk_bf16(float lo, float hi) { unsigned r; asm volatile("v_cvt_pk_bf16_f32 %0, %1, %2" : "=v"(r) : "v"(lo), "v"(hi)); return r; }
;     __device__ __forceinline__ bf16_t* Y() const { return (bf16_t*)(ws + WS_Y); }
;     __device__ __forceinline__ void operator()(const AccT& acc, const gm::GUnit& u, int wr, int wc, int fr, int fq) const {
;     ...
;                     const int slot = slots[ai * 4 + m];
;                     if (slot >= 0) {
;                         const float w = ws8[ai * 4 + m];
;                         bf16_t* yp = Y + (size_t)slot * DM + col;
; #pragma unroll
;                         for (int bj = 0; bj < 2; ++bj) {
;                             const f32x4 y0 = (acc[ai][bj][m][0] + bv[bj][0]) * w, y1 = (acc[ai][bj][m][1] + bv[bj][1]) * w;
;                             u32x4 q; q.x = cvt_pk_bf16(y0[0], y0[1]); q.y = cvt_pk_bf16(y0[2], y0[3]); q.z = cvt_pk_bf16(y1[0], y1[1]); q.w = cvt_pk_bf16(y1[2], y1[3]);
;                             *(u32x4*)(yp + bj * 128) = q;
;                         }
;                     }
.LBB0_1817:
	v_mov_b32_e32 v169, v147
	v_lshlrev_b64 v[168:169], 11, v[168:169]
	v_lshl_add_u64 v[168:169], s[44:45], 0, v[168:169]
	v_lshl_add_u64 v[172:173], v[148:149], 1, v[168:169]
	v_pk_add_f32 v[168:169], v[104:105], v[144:145]
	v_pk_add_f32 v[170:171], v[102:103], v[142:143]
	v_pk_mul_f32 v[174:175], v[168:169], v[166:167] op_sel_hi:[1,0]
	v_pk_mul_f32 v[168:169], v[170:171], v[166:167] op_sel_hi:[1,0]
	v_pk_add_f32 v[170:171], v[100:101], v[140:141]
	v_pk_add_f32 v[176:177], v[98:99], v[138:139]
	v_pk_mul_f32 v[178:179], v[170:171], v[166:167] op_sel_hi:[1,0]
	v_pk_mul_f32 v[170:171], v[176:177], v[166:167] op_sel_hi:[1,0]
	v_cvt_pk_bf16_f32 v168, v168, v169
	v_cvt_pk_bf16_f32 v169, v174, v175
	v_pk_add_f32 v[174:175], v[36:37], v[124:125]
	v_cvt_pk_bf16_f32 v170, v170, v171
	v_cvt_pk_bf16_f32 v171, v178, v179
	global_store_dwordx4 v[172:173], v[168:171], off nt
	v_pk_add_f32 v[176:177], v[34:35], v[122:123]
	v_pk_mul_f32 v[174:175], v[174:175], v[166:167] op_sel_hi:[1,0]
	v_pk_add_f32 v[168:169], v[40:41], v[128:129]
	v_pk_add_f32 v[170:171], v[38:39], v[126:127]
	v_pk_mul_f32 v[168:169], v[168:169], v[166:167] op_sel_hi:[1,0]
	v_pk_mul_f32 v[170:171], v[170:171], v[166:167] op_sel_hi:[1,0]
	v_pk_mul_f32 v[176:177], v[176:177], v[166:167] op_sel_hi:[1,0]
	v_cvt_pk_bf16_f32 v166, v170, v171
	v_cvt_pk_bf16_f32 v167, v168, v169
	s_nop 0
	v_cvt_pk_bf16_f32 v168, v176, v177
	v_cvt_pk_bf16_f32 v169, v174, v175
	global_store_dwordx4 v[172:173], v[166:169], off offset:256 nt
	s_or_b64 exec, exec, s[8:9]
	v_cmp_lt_i32_e32 vcc, -1, v164
	s_and_saveexec_b64 s[8:9], vcc
	s_cbranch_execz .LBB0_1806
.LBB0_1818:
	v_mov_b32_e32 v165, v147
	v_lshlrev_b64 v[164:165], 11, v[164:165]
	v_lshl_add_u64 v[164:165], s[44:45], 0, v[164:165]
	v_lshl_add_u64 v[168:169], v[148:149], 1, v[164:165]
	v_pk_add_f32 v[164:165], v[96:97], v[144:145]
	v_pk_add_f32 v[166:167], v[94:95], v[142:143]
	v_pk_mul_f32 v[170:171], v[164:165], v[162:163] op_sel_hi:[1,0]
	v_pk_mul_f32 v[164:165], v[166:167], v[162:163] op_sel_hi:[1,0]
	v_pk_add_f32 v[166:167], v[92:93], v[140:141]
	v_pk_add_f32 v[172:173], v[90:91], v[138:139]
	v_pk_mul_f32 v[174:175], v[166:167], v[162:163] op_sel_hi:[1,0]
	v_pk_mul_f32 v[166:167], v[172:173], v[162:163] op_sel_hi:[1,0]
	v_cvt_pk_bf16_f32 v164, v164, v165
	v_cvt_pk_bf16_f32 v165, v170, v171
	v_pk_add_f32 v[170:171], v[28:29], v[124:125]
	v_cvt_pk_bf16_f32 v166, v166, v167
	v_cvt_pk_bf16_f32 v167, v174, v175
	global_store_dwordx4 v[168:169], v[164:167], off nt
	v_pk_add_f32 v[172:173], v[26:27], v[122:123]
	v_pk_mul_f32 v[170:171], v[170:171], v[162:163] op_sel_hi:[1,0]
	v_pk_add_f32 v[164:165], v[32:33], v[128:129]
	v_pk_add_f32 v[166:167], v[30:31], v[126:127]
	v_pk_mul_f32 v[164:165], v[164:165], v[162:163] op_sel_hi:[1,0]
	v_pk_mul_f32 v[166:167], v[166:167], v[162:163] op_sel_hi:[1,0]
	v_pk_mul_f32 v[172:173], v[172:173], v[162:163] op_sel_hi:[1,0]
	v_cvt_pk_bf16_f32 v162, v166, v167
	v_cvt_pk_bf16_f32 v163, v164, v165
	s_nop 0
	v_cvt_pk_bf16_f32 v164, v172, v173
	v_cvt_pk_bf16_f32 v165, v170, v171
	global_store_dwordx4 v[168:169], v[162:165], off offset:256 nt
	s_or_b64 exec, exec, s[8:9]
	v_cmp_lt_i32_e32 vcc, -1, v160
	s_and_saveexec_b64 s[8:9], vcc
	s_cbranch_execz .LBB0_1807
; __device__ __forceinline__ unsigned cvt_pk_bf16(float lo, float hi) { unsigned r; asm volatile("v_cvt_pk_bf16_f32 %0, %1, %2" : "=v"(r) : "v"(lo), "v"(hi)); return r; }
;     __device__ __forceinline__ bf16_t* Y() const { return (bf16_t*)(ws + WS_Y); }
;     __device__ __forceinline__ void operator()(const AccT& acc, const gm::GUnit& u, int wr, int wc, int fr, int fq) const {
;     ...
;                     const int slot = slots[ai * 4 + m];
;                     if (slot >= 0) {
;                         const float w = ws8[ai * 4 + m];
;                         bf16_t* yp = Y + (size_t)slot * DM + col;
; #pragma unroll
;                         for (int bj = 0; bj < 2; ++bj) {
;                             const f32x4 y0 = (acc[ai][bj][m][0] + bv[bj][0]) * w, y1 = (acc[ai][bj][m][1] + bv[bj][1]) * w;
;                             u32x4 q; q.x = cvt_pk_bf16(y0[0], y0[1]); q.y = cvt_pk_bf16(y0[2], y0[3]); q.z = cvt_pk_bf16(y1[0], y1[1]); q.w = cvt_pk_bf16(y1[2], y1[3]);
;                             *(u32x4*)(yp + bj * 128) = q;
;                         }
;                     }
.LBB0_1819:
	v_mov_b32_e32 v161, v147
	v_lshlrev_b64 v[160:161], 11, v[160:161]
	v_lshl_add_u64 v[160:161], s[44:45], 0, v[160:161]
	v_lshl_add_u64 v[164:165], v[148:149], 1, v[160:161]
	v_pk_add_f32 v[160:161], v[88:89], v[144:145]
	v_pk_add_f32 v[162:163], v[86:87], v[142:143]
	v_pk_mul_f32 v[166:167], v[160:161], v[158:159] op_sel_hi:[1,0]
	v_pk_mul_f32 v[160:161], v[162:163], v[158:159] op_sel_hi:[1,0]
	v_pk_add_f32 v[162:163], v[84:85], v[140:141]
	v_pk_add_f32 v[168:169], v[82:83], v[138:139]
	v_pk_mul_f32 v[170:171], v[162:163], v[158:159] op_sel_hi:[1,0]
	v_pk_mul_f32 v[162:163], v[168:169], v[158:159] op_sel_hi:[1,0]
	v_cvt_pk_bf16_f32 v160, v160, v161
	v_cvt_pk_bf16_f32 v161, v166, v167
	v_pk_add_f32 v[166:167], v[20:21], v[124:125]
	v_cvt_pk_bf16_f32 v162, v162, v163
	v_cvt_pk_bf16_f32 v163, v170, v171
	global_store_dwordx4 v[164:165], v[160:163], off nt
	v_pk_add_f32 v[168:169], v[18:19], v[122:123]
	v_pk_mul_f32 v[166:167], v[166:167], v[158:159] op_sel_hi:[1,0]
	v_pk_add_f32 v[160:161], v[24:25], v[128:129]
	v_pk_add_f32 v[162:163], v[22:23], v[126:127]
	v_pk_mul_f32 v[160:161], v[160:161], v[158:159] op_sel_hi:[1,0]
	v_pk_mul_f32 v[162:163], v[162:163], v[158:159] op_sel_hi:[1,0]
	v_pk_mul_f32 v[168:169], v[168:169], v[158:159] op_sel_hi:[1,0]
	v_cvt_pk_bf16_f32 v158, v162, v163
	v_cvt_pk_bf16_f32 v159, v160, v161
	s_nop 0
	v_cvt_pk_bf16_f32 v160, v168, v169
	v_cvt_pk_bf16_f32 v161, v166, v167
	global_store_dwordx4 v[164:165], v[158:161], off offset:256 nt
	s_or_b64 exec, exec, s[8:9]
	v_cmp_lt_i32_e32 vcc, -1, v156
	s_and_saveexec_b64 s[8:9], vcc
	s_cbranch_execz .LBB0_1808
.LBB0_1820:
	v_mov_b32_e32 v157, v147
	v_lshlrev_b64 v[156:157], 11, v[156:157]
	v_lshl_add_u64 v[156:157], s[44:45], 0, v[156:157]
	v_lshl_add_u64 v[160:161], v[148:149], 1, v[156:157]
	v_pk_add_f32 v[156:157], v[80:81], v[144:145]
	v_pk_add_f32 v[158:159], v[78:79], v[142:143]
	v_pk_mul_f32 v[162:163], v[156:157], v[154:155] op_sel_hi:[1,0]
	v_pk_mul_f32 v[156:157], v[158:159], v[154:155] op_sel_hi:[1,0]
	v_pk_add_f32 v[158:159], v[76:77], v[140:141]
	v_pk_add_f32 v[164:165], v[74:75], v[138:139]
	v_pk_mul_f32 v[166:167], v[158:159], v[154:155] op_sel_hi:[1,0]
	v_pk_mul_f32 v[158:159], v[164:165], v[154:155] op_sel_hi:[1,0]
	v_cvt_pk_bf16_f32 v156, v156, v157
	v_cvt_pk_bf16_f32 v157, v162, v163
	v_pk_add_f32 v[164:165], v[10:11], v[122:123]
	v_cvt_pk_bf16_f32 v158, v158, v159
	v_cvt_pk_bf16_f32 v159, v166, v167
	global_store_dwordx4 v[160:161], v[156:159], off nt
	s_nop 1
	v_pk_add_f32 v[156:157], v[16:17], v[128:129]
	v_pk_add_f32 v[158:159], v[14:15], v[126:127]
	v_pk_mul_f32 v[162:163], v[156:157], v[154:155] op_sel_hi:[1,0]
	v_pk_mul_f32 v[156:157], v[158:159], v[154:155] op_sel_hi:[1,0]
	v_pk_add_f32 v[158:159], v[12:13], v[124:125]
	v_cvt_pk_bf16_f32 v156, v156, v157
	v_cvt_pk_bf16_f32 v157, v162, v163
	s_nop 0
	v_pk_mul_f32 v[166:167], v[158:159], v[154:155] op_sel_hi:[1,0]
	v_pk_mul_f32 v[158:159], v[164:165], v[154:155] op_sel_hi:[1,0]
	s_nop 0
	v_cvt_pk_bf16_f32 v158, v158, v159
	v_cvt_pk_bf16_f32 v159, v166, v167
	global_store_dwordx4 v[160:161], v[156:159], off offset:256 nt
	s_or_b64 exec, exec, s[8:9]
	v_cmp_lt_i32_e32 vcc, -1, v152
	s_and_saveexec_b64 s[8:9], vcc
	s_cbranch_execz .LBB0_1809
.LBB0_1821:
	v_mov_b32_e32 v153, v147
	v_lshlrev_b64 v[152:153], 11, v[152:153]
	v_lshl_add_u64 v[152:153], s[44:45], 0, v[152:153]
	v_pk_add_f32 v[144:145], v[72:73], v[144:145]
	v_pk_add_f32 v[142:143], v[70:71], v[142:143]
	v_pk_add_f32 v[140:141], v[68:69], v[140:141]
	v_pk_add_f32 v[138:139], v[66:67], v[138:139]
	v_lshl_add_u64 v[148:149], v[148:149], 1, v[152:153]
	v_pk_mul_f32 v[144:145], v[144:145], v[150:151] op_sel_hi:[1,0]
	v_pk_mul_f32 v[142:143], v[142:143], v[150:151] op_sel_hi:[1,0]
	v_pk_mul_f32 v[152:153], v[140:141], v[150:151] op_sel_hi:[1,0]
	v_pk_mul_f32 v[140:141], v[138:139], v[150:151] op_sel_hi:[1,0]
	v_cvt_pk_bf16_f32 v138, v142, v143
	v_cvt_pk_bf16_f32 v139, v144, v145
	v_pk_add_f32 v[124:125], v[4:5], v[124:125]
	v_pk_add_f32 v[122:123], v[2:3], v[122:123]
	v_cvt_pk_bf16_f32 v140, v140, v141
	v_cvt_pk_bf16_f32 v141, v152, v153
	global_store_dwordx4 v[148:149], v[138:141], off nt
	v_pk_add_f32 v[128:129], v[8:9], v[128:129]
	v_pk_add_f32 v[126:127], v[6:7], v[126:127]
	v_pk_mul_f32 v[138:139], v[124:125], v[150:151] op_sel_hi:[1,0]
	v_pk_mul_f32 v[124:125], v[122:123], v[150:151] op_sel_hi:[1,0]
	v_pk_mul_f32 v[128:129], v[128:129], v[150:151] op_sel_hi:[1,0]
	v_pk_mul_f32 v[126:127], v[126:127], v[150:151] op_sel_hi:[1,0]
	s_nop 0
	v_cvt_pk_bf16_f32 v122, v126, v127
	v_cvt_pk_bf16_f32 v123, v128, v129
	v_cvt_pk_bf16_f32 v124, v124, v125
	v_cvt_pk_bf16_f32 v125, v138, v139
	global_store_dwordx4 v[148:149], v[122:125], off offset:256 nt
	s_or_b64 exec, exec, s[8:9]
	s_cmp_lg_u32 s7, 11
	s_cbranch_scc0 .LBB0_1810
	s_branch .LBB0_1811

; __device__ __forceinline__ unsigned cvt_pk_bf16(float lo, float hi) { unsigned r; asm volatile("v_cvt_pk_bf16_f32 %0, %1, %2" : "=v"(r) : "v"(lo), "v"(hi)); return r; }
;     __device__ __forceinline__ bf16_t* Y() const { return (bf16_t*)(ws + WS_Y); }
;     __device__ __forceinline__ void operator()(const AccT& acc, const gm::GUnit& u, int wr, int wc, int fr, int fq) const {
;     ...
;                     const int slot = slots[ai * 4 + m];
;                     if (slot >= 0) {
;                         const float w = ws8[ai * 4 + m];
;                         bf16_t* yp = Y + (size_t)slot * DM + col;
; #pragma unroll
;                         for (int bj = 0; bj < 2; ++bj) {
;                             const f32x4 y0 = (acc[ai][bj][m][0] + bv[bj][0]) * w, y1 = (acc[ai][bj][m][1] + bv[bj][1]) * w;
;                             u32x4 q; q.x = cvt_pk_bf16(y0[0], y0[1]); q.y = cvt_pk_bf16(y0[2], y0[3]); q.z = cvt_pk_bf16(y1[0], y1[1]); q.w = cvt_pk_bf16(y1[2], y1[3]);
;                             *(u32x4*)(yp + bj * 128) = q;
;                         }
;                     }
.LBB0_1865:
	v_mov_b32_e32 v153, v147
	v_lshlrev_b64 v[152:153], 11, v[152:153]
	v_lshl_add_u64 v[152:153], s[44:45], 0, v[152:153]
	v_pk_add_f32 v[144:145], v[72:73], v[144:145]
	v_pk_add_f32 v[142:143], v[70:71], v[142:143]
	v_pk_add_f32 v[140:141], v[68:69], v[140:141]
	v_pk_add_f32 v[138:139], v[66:67], v[138:139]
	v_lshl_add_u64 v[148:149], v[148:149], 1, v[152:153]
	v_pk_mul_f32 v[144:145], v[144:145], v[150:151] op_sel_hi:[1,0]
	v_pk_mul_f32 v[142:143], v[142:143], v[150:151] op_sel_hi:[1,0]
	v_pk_mul_f32 v[152:153], v[140:141], v[150:151] op_sel_hi:[1,0]
	v_pk_mul_f32 v[140:141], v[138:139], v[150:151] op_sel_hi:[1,0]
	v_cvt_pk_bf16_f32 v138, v142, v143
	v_cvt_pk_bf16_f32 v139, v144, v145
	v_pk_add_f32 v[132:133], v[4:5], v[132:133]
	v_pk_add_f32 v[130:131], v[2:3], v[130:131]
	v_cvt_pk_bf16_f32 v140, v140, v141
	v_cvt_pk_bf16_f32 v141, v152, v153
	global_store_dwordx4 v[148:149], v[138:141], off nt
	v_pk_add_f32 v[136:137], v[8:9], v[136:137]
	v_pk_add_f32 v[134:135], v[6:7], v[134:135]
	v_pk_mul_f32 v[138:139], v[132:133], v[150:151] op_sel_hi:[1,0]
	v_pk_mul_f32 v[132:133], v[130:131], v[150:151] op_sel_hi:[1,0]
	v_pk_mul_f32 v[136:137], v[136:137], v[150:151] op_sel_hi:[1,0]
	v_pk_mul_f32 v[134:135], v[134:135], v[150:151] op_sel_hi:[1,0]
	s_nop 0
	v_cvt_pk_bf16_f32 v130, v134, v135
	v_cvt_pk_bf16_f32 v131, v136, v137
	v_cvt_pk_bf16_f32 v132, v132, v133
	v_cvt_pk_bf16_f32 v133, v138, v139
	global_store_dwordx4 v[148:149], v[130:133], off offset:256 nt

; __device__ __forceinline__ unsigned cvt_pk_bf16(float lo, float hi) { unsigned r; asm volatile("v_cvt_pk_bf16_f32 %0, %1, %2" : "=v"(r) : "v"(lo), "v"(hi)); return r; }
;     __device__ __forceinline__ bf16_t* Y() const { return (bf16_t*)(ws + WS_Y); }
;     __device__ __forceinline__ void operator()(const AccT& acc, const gm::GUnit& u, int wr, int wc, int fr, int fq) const {
;     ...
;                     const int slot = slots[ai * 4 + m];
;                     if (slot >= 0) {
;                         const float w = ws8[ai * 4 + m];
;                         bf16_t* yp = Y + (size_t)slot * DM + col;
; #pragma unroll
;                         for (int bj = 0; bj < 2; ++bj) {
;                             const f32x4 y0 = (acc[ai][bj][m][0] + bv[bj][0]) * w, y1 = (acc[ai][bj][m][1] + bv[bj][1]) * w;
;                             u32x4 q; q.x = cvt_pk_bf16(y0[0], y0[1]); q.y = cvt_pk_bf16(y0[2], y0[3]); q.z = cvt_pk_bf16(y1[0], y1[1]); q.w = cvt_pk_bf16(y1[2], y1[3]);
;                             *(u32x4*)(yp + bj * 128) = q;
;                         }
;                     }
.LBB0_1869:
	v_mov_b32_e32 v191, v147
	v_lshlrev_b64 v[190:191], 11, v[190:191]
	v_pk_add_f32 v[200:201], v[126:127], v[142:143]
	v_lshl_add_u64 v[190:191], s[44:45], 0, v[190:191]
	v_pk_add_f32 v[194:195], v[128:129], v[144:145]
	v_pk_mul_f32 v[200:201], v[200:201], v[178:179] op_sel_hi:[1,0]
	v_pk_add_f32 v[202:203], v[124:125], v[140:141]
	v_pk_add_f32 v[204:205], v[122:123], v[138:139]
	v_lshl_add_u64 v[190:191], v[148:149], 1, v[190:191]
	v_pk_mul_f32 v[194:195], v[194:195], v[178:179] op_sel_hi:[1,0]
	v_pk_mul_f32 v[206:207], v[202:203], v[178:179] op_sel_hi:[1,0]
	v_pk_mul_f32 v[202:203], v[204:205], v[178:179] op_sel_hi:[1,0]
	v_cvt_pk_bf16_f32 v200, v200, v201
	v_cvt_pk_bf16_f32 v201, v194, v195
	v_pk_add_f32 v[194:195], v[64:65], v[136:137]
	v_cvt_pk_bf16_f32 v202, v202, v203
	v_cvt_pk_bf16_f32 v203, v206, v207
	global_store_dwordx4 v[190:191], v[200:203], off nt
	v_pk_add_f32 v[204:205], v[58:59], v[130:131]
	v_pk_mul_f32 v[194:195], v[194:195], v[178:179] op_sel_hi:[1,0]
	v_pk_add_f32 v[200:201], v[62:63], v[134:135]
	v_pk_add_f32 v[202:203], v[60:61], v[132:133]
	v_pk_mul_f32 v[200:201], v[200:201], v[178:179] op_sel_hi:[1,0]
	v_pk_mul_f32 v[206:207], v[202:203], v[178:179] op_sel_hi:[1,0]
	v_pk_mul_f32 v[178:179], v[204:205], v[178:179] op_sel_hi:[1,0]
	v_cvt_pk_bf16_f32 v200, v200, v201
	v_cvt_pk_bf16_f32 v201, v194, v195
	s_nop 0
	v_cvt_pk_bf16_f32 v202, v178, v179
	v_cvt_pk_bf16_f32 v203, v206, v207
	global_store_dwordx4 v[190:191], v[200:203], off offset:256 nt
	s_or_b64 exec, exec, s[8:9]
	v_cmp_lt_i32_e32 vcc, -1, v176
	s_and_saveexec_b64 s[8:9], vcc
	s_cbranch_execz .LBB0_1859
.LBB0_1870:
	v_mov_b32_e32 v177, v147
	v_lshlrev_b64 v[176:177], 11, v[176:177]
	v_lshl_add_u64 v[176:177], s[44:45], 0, v[176:177]
	v_lshl_add_u64 v[190:191], v[148:149], 1, v[176:177]
	v_pk_add_f32 v[176:177], v[120:121], v[144:145]
	v_pk_add_f32 v[178:179], v[118:119], v[142:143]
	v_pk_mul_f32 v[194:195], v[176:177], v[174:175] op_sel_hi:[1,0]
	v_pk_mul_f32 v[176:177], v[178:179], v[174:175] op_sel_hi:[1,0]
	v_pk_add_f32 v[178:179], v[116:117], v[140:141]
	v_pk_add_f32 v[200:201], v[114:115], v[138:139]
	v_pk_mul_f32 v[202:203], v[178:179], v[174:175] op_sel_hi:[1,0]
	v_pk_mul_f32 v[178:179], v[200:201], v[174:175] op_sel_hi:[1,0]
	v_cvt_pk_bf16_f32 v176, v176, v177
	v_cvt_pk_bf16_f32 v177, v194, v195
	v_pk_add_f32 v[194:195], v[52:53], v[132:133]
	v_cvt_pk_bf16_f32 v178, v178, v179
	v_cvt_pk_bf16_f32 v179, v202, v203
	global_store_dwordx4 v[190:191], v[176:179], off nt
	v_pk_add_f32 v[200:201], v[50:51], v[130:131]
	v_pk_mul_f32 v[194:195], v[194:195], v[174:175] op_sel_hi:[1,0]
	v_pk_add_f32 v[176:177], v[56:57], v[136:137]
	v_pk_add_f32 v[178:179], v[54:55], v[134:135]
	v_pk_mul_f32 v[176:177], v[176:177], v[174:175] op_sel_hi:[1,0]
	v_pk_mul_f32 v[178:179], v[178:179], v[174:175] op_sel_hi:[1,0]
	v_pk_mul_f32 v[200:201], v[200:201], v[174:175] op_sel_hi:[1,0]
	v_cvt_pk_bf16_f32 v174, v178, v179
	v_cvt_pk_bf16_f32 v175, v176, v177
	s_nop 0
	v_cvt_pk_bf16_f32 v176, v200, v201
	v_cvt_pk_bf16_f32 v177, v194, v195
	global_store_dwordx4 v[190:191], v[174:177], off offset:256 nt
	s_or_b64 exec, exec, s[8:9]
	v_cmp_lt_i32_e32 vcc, -1, v172
	s_and_saveexec_b64 s[8:9], vcc
	s_cbranch_execz .LBB0_1860
.LBB0_1871:
	v_mov_b32_e32 v173, v147
	v_lshlrev_b64 v[172:173], 11, v[172:173]
	v_lshl_add_u64 v[172:173], s[44:45], 0, v[172:173]
	v_lshl_add_u64 v[176:177], v[148:149], 1, v[172:173]
	v_pk_add_f32 v[172:173], v[112:113], v[144:145]
	v_pk_add_f32 v[174:175], v[110:111], v[142:143]
	v_pk_mul_f32 v[178:179], v[172:173], v[170:171] op_sel_hi:[1,0]
	v_pk_mul_f32 v[172:173], v[174:175], v[170:171] op_sel_hi:[1,0]
	v_pk_add_f32 v[174:175], v[108:109], v[140:141]
	v_pk_add_f32 v[190:191], v[106:107], v[138:139]
	v_pk_mul_f32 v[194:195], v[174:175], v[170:171] op_sel_hi:[1,0]
	v_pk_mul_f32 v[174:175], v[190:191], v[170:171] op_sel_hi:[1,0]
	v_cvt_pk_bf16_f32 v172, v172, v173
	v_cvt_pk_bf16_f32 v173, v178, v179
	v_pk_add_f32 v[178:179], v[44:45], v[132:133]
	v_cvt_pk_bf16_f32 v174, v174, v175
	v_cvt_pk_bf16_f32 v175, v194, v195
	global_store_dwordx4 v[176:177], v[172:175], off nt
	v_pk_add_f32 v[190:191], v[42:43], v[130:131]
	v_pk_mul_f32 v[178:179], v[178:179], v[170:171] op_sel_hi:[1,0]
	v_pk_add_f32 v[172:173], v[48:49], v[136:137]
	v_pk_add_f32 v[174:175], v[46:47], v[134:135]
	v_pk_mul_f32 v[172:173], v[172:173], v[170:171] op_sel_hi:[1,0]
	v_pk_mul_f32 v[174:175], v[174:175], v[170:171] op_sel_hi:[1,0]
	v_pk_mul_f32 v[190:191], v[190:191], v[170:171] op_sel_hi:[1,0]
	v_cvt_pk_bf16_f32 v170, v174, v175
	v_cvt_pk_bf16_f32 v171, v172, v173
	s_nop 0
	v_cvt_pk_bf16_f32 v172, v190, v191
	v_cvt_pk_bf16_f32 v173, v178, v179
	global_store_dwordx4 v[176:177], v[170:173], off offset:256 nt
	s_or_b64 exec, exec, s[8:9]
	v_cmp_lt_i32_e32 vcc, -1, v168
	s_and_saveexec_b64 s[8:9], vcc
	s_cbranch_execz .LBB0_1861
; __device__ __forceinline__ unsigned cvt_pk_bf16(float lo, float hi) { unsigned r; asm volatile("v_cvt_pk_bf16_f32 %0, %1, %2" : "=v"(r) : "v"(lo), "v"(hi)); return r; }
;     __device__ __forceinline__ bf16_t* Y() const { return (bf16_t*)(ws + WS_Y); }
;     __device__ __forceinline__ void operator()(const AccT& acc, const gm::GUnit& u, int wr, int wc, int fr, int fq) const {
;     ...
;                     const int slot = slots[ai * 4 + m];
;                     if (slot >= 0) {
;                         const float w = ws8[ai * 4 + m];
;                         bf16_t* yp = Y + (size_t)slot * DM + col;
; #pragma unroll
;                         for (int bj = 0; bj < 2; ++bj) {
;                             const f32x4 y0 = (acc[ai][bj][m][0] + bv[bj][0]) * w, y1 = (acc[ai][bj][m][1] + bv[bj][1]) * w;
;                             u32x4 q; q.x = cvt_pk_bf16(y0[0], y0[1]); q.y = cvt_pk_bf16(y0[2], y0[3]); q.z = cvt_pk_bf16(y1[0], y1[1]); q.w = cvt_pk_bf16(y1[2], y1[3]);
;                             *(u32x4*)(yp + bj * 128) = q;
;                         }
;                     }
.LBB0_1872:
	v_mov_b32_e32 v169, v147
	v_lshlrev_b64 v[168:169], 11, v[168:169]
	v_lshl_add_u64 v[168:169], s[44:45], 0, v[168:169]
	v_lshl_add_u64 v[172:173], v[148:149], 1, v[168:169]
	v_pk_add_f32 v[168:169], v[104:105], v[144:145]
	v_pk_add_f32 v[170:171], v[102:103], v[142:143]
	v_pk_mul_f32 v[174:175], v[168:169], v[166:167] op_sel_hi:[1,0]
	v_pk_mul_f32 v[168:169], v[170:171], v[166:167] op_sel_hi:[1,0]
	v_pk_add_f32 v[170:171], v[100:101], v[140:141]
	v_pk_add_f32 v[176:177], v[98:99], v[138:139]
	v_pk_mul_f32 v[178:179], v[170:171], v[166:167] op_sel_hi:[1,0]
	v_pk_mul_f32 v[170:171], v[176:177], v[166:167] op_sel_hi:[1,0]
	v_cvt_pk_bf16_f32 v168, v168, v169
	v_cvt_pk_bf16_f32 v169, v174, v175
	v_pk_add_f32 v[174:175], v[36:37], v[132:133]
	v_cvt_pk_bf16_f32 v170, v170, v171
	v_cvt_pk_bf16_f32 v171, v178, v179
	global_store_dwordx4 v[172:173], v[168:171], off nt
	v_pk_add_f32 v[176:177], v[34:35], v[130:131]
	v_pk_mul_f32 v[174:175], v[174:175], v[166:167] op_sel_hi:[1,0]
	v_pk_add_f32 v[168:169], v[40:41], v[136:137]
	v_pk_add_f32 v[170:171], v[38:39], v[134:135]
	v_pk_mul_f32 v[168:169], v[168:169], v[166:167] op_sel_hi:[1,0]
	v_pk_mul_f32 v[170:171], v[170:171], v[166:167] op_sel_hi:[1,0]
	v_pk_mul_f32 v[176:177], v[176:177], v[166:167] op_sel_hi:[1,0]
	v_cvt_pk_bf16_f32 v166, v170, v171
	v_cvt_pk_bf16_f32 v167, v168, v169
	s_nop 0
	v_cvt_pk_bf16_f32 v168, v176, v177
	v_cvt_pk_bf16_f32 v169, v174, v175
	global_store_dwordx4 v[172:173], v[166:169], off offset:256 nt
	s_or_b64 exec, exec, s[8:9]
	v_cmp_lt_i32_e32 vcc, -1, v164
	s_and_saveexec_b64 s[8:9], vcc
	s_cbranch_execz .LBB0_1862
.LBB0_1873:
	v_mov_b32_e32 v165, v147
	v_lshlrev_b64 v[164:165], 11, v[164:165]
	v_lshl_add_u64 v[164:165], s[44:45], 0, v[164:165]
	v_lshl_add_u64 v[168:169], v[148:149], 1, v[164:165]
	v_pk_add_f32 v[164:165], v[96:97], v[144:145]
	v_pk_add_f32 v[166:167], v[94:95], v[142:143]
	v_pk_mul_f32 v[170:171], v[164:165], v[162:163] op_sel_hi:[1,0]
	v_pk_mul_f32 v[164:165], v[166:167], v[162:163] op_sel_hi:[1,0]
	v_pk_add_f32 v[166:167], v[92:93], v[140:141]
	v_pk_add_f32 v[172:173], v[90:91], v[138:139]
	v_pk_mul_f32 v[174:175], v[166:167], v[162:163] op_sel_hi:[1,0]
	v_pk_mul_f32 v[166:167], v[172:173], v[162:163] op_sel_hi:[1,0]
	v_cvt_pk_bf16_f32 v164, v164, v165
	v_cvt_pk_bf16_f32 v165, v170, v171
	v_pk_add_f32 v[170:171], v[28:29], v[132:133]
	v_cvt_pk_bf16_f32 v166, v166, v167
	v_cvt_pk_bf16_f32 v167, v174, v175
	global_store_dwordx4 v[168:169], v[164:167], off nt
	v_pk_add_f32 v[172:173], v[26:27], v[130:131]
	v_pk_mul_f32 v[170:171], v[170:171], v[162:163] op_sel_hi:[1,0]
	v_pk_add_f32 v[164:165], v[32:33], v[136:137]
	v_pk_add_f32 v[166:167], v[30:31], v[134:135]
	v_pk_mul_f32 v[164:165], v[164:165], v[162:163] op_sel_hi:[1,0]
	v_pk_mul_f32 v[166:167], v[166:167], v[162:163] op_sel_hi:[1,0]
	v_pk_mul_f32 v[172:173], v[172:173], v[162:163] op_sel_hi:[1,0]
	v_cvt_pk_bf16_f32 v162, v166, v167
	v_cvt_pk_bf16_f32 v163, v164, v165
	s_nop 0
	v_cvt_pk_bf16_f32 v164, v172, v173
	v_cvt_pk_bf16_f32 v165, v170, v171
	global_store_dwordx4 v[168:169], v[162:165], off offset:256 nt
	s_or_b64 exec, exec, s[8:9]
	v_cmp_lt_i32_e32 vcc, -1, v160
	s_and_saveexec_b64 s[8:9], vcc
	s_cbranch_execz .LBB0_1863
.LBB0_1874:
	v_mov_b32_e32 v161, v147
	v_lshlrev_b64 v[160:161], 11, v[160:161]
	v_lshl_add_u64 v[160:161], s[44:45], 0, v[160:161]
	v_lshl_add_u64 v[164:165], v[148:149], 1, v[160:161]
	v_pk_add_f32 v[160:161], v[88:89], v[144:145]
	v_pk_add_f32 v[162:163], v[86:87], v[142:143]
	v_pk_mul_f32 v[166:167], v[160:161], v[158:159] op_sel_hi:[1,0]
	v_pk_mul_f32 v[160:161], v[162:163], v[158:159] op_sel_hi:[1,0]
	v_pk_add_f32 v[162:163], v[84:85], v[140:141]
	v_pk_add_f32 v[168:169], v[82:83], v[138:139]
	v_pk_mul_f32 v[170:171], v[162:163], v[158:159] op_sel_hi:[1,0]
	v_pk_mul_f32 v[162:163], v[168:169], v[158:159] op_sel_hi:[1,0]
	v_cvt_pk_bf16_f32 v160, v160, v161
	v_cvt_pk_bf16_f32 v161, v166, v167
	v_pk_add_f32 v[166:167], v[20:21], v[132:133]
	v_cvt_pk_bf16_f32 v162, v162, v163
	v_cvt_pk_bf16_f32 v163, v170, v171
	global_store_dwordx4 v[164:165], v[160:163], off nt
	v_pk_add_f32 v[168:169], v[18:19], v[130:131]
	v_pk_mul_f32 v[166:167], v[166:167], v[158:159] op_sel_hi:[1,0]
	v_pk_add_f32 v[160:161], v[24:25], v[136:137]
	v_pk_add_f32 v[162:163], v[22:23], v[134:135]
	v_pk_mul_f32 v[160:161], v[160:161], v[158:159] op_sel_hi:[1,0]
	v_pk_mul_f32 v[162:163], v[162:163], v[158:159] op_sel_hi:[1,0]
	v_pk_mul_f32 v[168:169], v[168:169], v[158:159] op_sel_hi:[1,0]
	v_cvt_pk_bf16_f32 v158, v162, v163
	v_cvt_pk_bf16_f32 v159, v160, v161
	s_nop 0
	v_cvt_pk_bf16_f32 v160, v168, v169
	v_cvt_pk_bf16_f32 v161, v166, v167
	global_store_dwordx4 v[164:165], v[158:161], off offset:256 nt
	s_or_b64 exec, exec, s[8:9]
	v_cmp_lt_i32_e32 vcc, -1, v156
	s_and_saveexec_b64 s[8:9], vcc
	s_cbranch_execz .LBB0_1864
.LBB0_1875:
	v_mov_b32_e32 v157, v147
	v_lshlrev_b64 v[156:157], 11, v[156:157]
	v_lshl_add_u64 v[156:157], s[44:45], 0, v[156:157]
	v_lshl_add_u64 v[160:161], v[148:149], 1, v[156:157]
	v_pk_add_f32 v[156:157], v[80:81], v[144:145]
	v_pk_add_f32 v[158:159], v[78:79], v[142:143]
	v_pk_mul_f32 v[162:163], v[156:157], v[154:155] op_sel_hi:[1,0]
	v_pk_mul_f32 v[156:157], v[158:159], v[154:155] op_sel_hi:[1,0]
	v_pk_add_f32 v[158:159], v[76:77], v[140:141]
	v_pk_add_f32 v[164:165], v[74:75], v[138:139]
	v_pk_mul_f32 v[166:167], v[158:159], v[154:155] op_sel_hi:[1,0]
	v_pk_mul_f32 v[158:159], v[164:165], v[154:155] op_sel_hi:[1,0]
	v_cvt_pk_bf16_f32 v156, v156, v157
	v_cvt_pk_bf16_f32 v157, v162, v163
	v_pk_add_f32 v[164:165], v[10:11], v[130:131]
	v_cvt_pk_bf16_f32 v158, v158, v159
	v_cvt_pk_bf16_f32 v159, v166, v167
	global_store_dwordx4 v[160:161], v[156:159], off nt
	s_nop 1
	v_pk_add_f32 v[156:157], v[16:17], v[136:137]
	v_pk_add_f32 v[158:159], v[14:15], v[134:135]
	v_pk_mul_f32 v[162:163], v[156:157], v[154:155] op_sel_hi:[1,0]
	v_pk_mul_f32 v[156:157], v[158:159], v[154:155] op_sel_hi:[1,0]
	v_pk_add_f32 v[158:159], v[12:13], v[132:133]
	v_cvt_pk_bf16_f32 v156, v156, v157
	v_cvt_pk_bf16_f32 v157, v162, v163
	s_nop 0
	v_pk_mul_f32 v[166:167], v[158:159], v[154:155] op_sel_hi:[1,0]
	v_pk_mul_f32 v[158:159], v[164:165], v[154:155] op_sel_hi:[1,0]
	s_nop 0
	v_cvt_pk_bf16_f32 v158, v158, v159
	v_cvt_pk_bf16_f32 v159, v166, v167
	global_store_dwordx4 v[160:161], v[156:159], off offset:256 nt
	s_or_b64 exec, exec, s[8:9]
	v_cmp_lt_i32_e32 vcc, -1, v152
	s_and_saveexec_b64 s[8:9], vcc
	s_cbranch_execnz .LBB0_1865
	s_branch .LBB0_1866
